# combined: v11 + wide8 QK eight-reads-upfront + wide8 L-path PV four-set read rotation + dead zero-mov and self-max canonicalisation removal in attention loops + hand-written final-RMSNorm row loop
# speedup vs baseline: 1.0036x; 1.0036x over previous
; #define SBAR() __builtin_amdgcn_sched_barrier(0)
; #define VMW() asm volatile("s_waitcnt vmcnt(0)" ::: "memory")
; #define SWRITE_HV(bf) do { if constexpr (F8) { *(bf16x8*)(V_lds + (bf) * SHM_V + vws8) = S.st_v0; }                                                          \
;                            else { *(bf16x8*)(V_lds + (bf) * SHM_V + vst0) = S.st_v0; *(bf16x8*)(V_lds + (bf) * SHM_V + vst1) = S.st_v1; } } while (0)
; #define SWRITE_H(bf) do { SWRITE_HV(bf); SWRITE_HK(bf); } while (0)
; #define PSM(P0_, P1_, mn_, al_) partialSM<F8 ? 8 : 0, F8 ? 2 : 8, F8 ? 5 : 0>(P0_, P1_, m_reg, mn_, al_, dead_)
;     float pmax;
;     { float m0 = fmaxf(p0[0], p0[1]), m1 = fmaxf(p0[2], p0[3]), m2 = fmaxf(p1[0], p1[1]), m3 = fmaxf(p1[2], p1[3]);
; #pragma unroll
;       for (int r = 4; r < 16; r += 4) { m0 = fmaxf(fmaxf(m0, p0[r]), p0[r + 1]); m1 = fmaxf(fmaxf(m1, p0[r + 2]), p0[r + 3]); m2 = fmaxf(fmaxf(m2, p1[r]), p1[r + 1]); m3 = fmaxf(fmaxf(m3, p1[r + 2]), p1[r + 3]); }
;       pmax = fmaxf(fmaxf(m0, m1), fmaxf(m2, m3)); }
;     pmax = dead ? -__builtin_inff() : pmax;
;     { auto rr = __builtin_amdgcn_permlane32_swap(__float_as_uint(pmax), __float_as_uint(pmax), false, false);
;       pmax = fmaxf(__uint_as_float(rr[0]), __uint_as_float(rr[1])); }
;     constexpr float SCL = SCALE / (float)(1 << SH), C2 = 1.4426950408889634f * SCL;
;     if (__builtin_expect(__all((pmax - m_reg) * SCL <= (float)THRI), 1)) { mn = m_reg; alpha = 1.f; }
;     else { mn = fmaxf(m_reg, pmax); alpha = __builtin_amdgcn_exp2f((m_reg - mn) * C2); m_reg = mn; }
;     const float mnL = dead ? -__builtin_inff() : -mn * C2 + (float)PSH;
;     for (int r = 0; r < 16; ++r) p0[r] = fmaf(p0[r], C2, mnL); for (int r = 0; r < 16; ++r) p1[r] = fmaf(p1[r], C2, mnL);
; template <class Epi, bool F8 = false>
; __device__ __forceinline__ void block(const BlockRef& cur, int skv, char* lds, Seam& S, bool moba, unsigned selmask, const Epi& E) {
;     ...
;     f32x16 pA0, pA1, pB0, pB1; float mnA, mnB, alA, alB; bf16x8 pa0, pa1, pa2, pa3;
;     SWRITE_HV(0); SBAR();
;     if (NT > 1) SLOAD_H(Kh, Vh, KBASE(1));
;     SBAR(); QKT(0, pA0, pA1);
;     MASKT(pA0, pA1, 0); PSM(pA0, pA1, mnA, alA);
;     if (NT > 1) { VMW(); SWRITE_H(1); }
;     __syncthreads();
.LBB0_1045:
	s_add_i32 s8, s90, 0xffffff80
	s_cmp_lt_u32 s8, s72
	s_cselect_b64 s[6:7], -1, 0
	s_lshr_b32 s8, s8, 8
	s_lshl_b32 s8, 1, s8
	v_and_b32_e32 v13, s8, v131
	v_cmp_eq_u32_e32 vcc, 0, v13
	v_max_f32_e32 v13, v98, v99
	v_max_f32_e32 v15, v100, v101
	v_max_f32_e32 v16, v84, v85
	v_max3_f32 v17, v82, v83, v86
	v_max3_f32 v16, v16, v88, v89
	v_max3_f32 v13, v13, v102, v103
	v_max3_f32 v15, v15, v104, v105
	v_max3_f32 v17, v17, v87, v90
	v_max3_f32 v16, v16, v92, v93
	v_max3_f32 v13, v13, v106, v107
	v_max3_f32 v15, v15, v108, v109
	v_max3_f32 v17, v17, v91, v94
	v_max3_f32 v16, v16, v96, v97
	v_max3_f32 v13, v13, v110, v111
	v_max3_f32 v15, v15, v112, v113
	v_max3_f32 v16, v17, v95, v16
	v_max3_f32 v13, v13, v15, v16
	s_and_b64 s[6:7], s[6:7], vcc
	v_cndmask_b32_e64 v13, v13, v210, s[6:7]
	v_mov_b32_e32 v15, v13
	s_nop 1
	v_permlane32_swap_b32_e32 v13, v15
	v_max_f32_e32 v13, v13, v15
	v_sub_f32_e32 v15, v13, v163
	v_max_f32_e32 v13, v163, v13
	v_sub_f32_e32 v16, v163, v13
	v_mul_f32_e32 v16, 0x3a0293ee, v16
	v_mul_f32_e32 v15, 0x39b504f3, v15
	v_exp_f32_e32 v16, v16
	v_cmp_ge_f32_e32 vcc, 2.0, v15
	s_cmp_eq_u64 vcc, exec
	s_cselect_b64 s[8:9], -1, 0
	s_barrier
	s_waitcnt vmcnt(0)
	v_cndmask_b32_e64 v15, v16, 1.0, s[8:9]
	v_cmp_gt_f32_e32 vcc, 1.0, v15
	s_waitcnt vmcnt(1)
	ds_write_b128 v160, v[4:7]
	s_waitcnt vmcnt(0)
	ds_write_b128 v161, v[8:11] offset:32768
	s_cbranch_vccz .LBB0_1049
	s_and_saveexec_b64 s[10:11], s[4:5]
	ds_write_b32 v155, v15 offset:128
	s_or_b64 exec, exec, s[10:11]
	s_waitcnt lgkmcnt(0)
	v_add_u32_e32 v16, s73, v154
	ds_read_b128 v[136:139], v16 offset:224
	ds_read_b128 v[140:143], v16 offset:192
	ds_read_b128 v[144:147], v16 offset:160
	ds_read_b128 v[148:151], v16 offset:128
	s_waitcnt lgkmcnt(3)
	v_pk_mul_f32 v[46:47], v[46:47], v[136:137]
	s_waitcnt lgkmcnt(2)
	v_pk_mul_f32 v[42:43], v[42:43], v[140:141]
	s_waitcnt lgkmcnt(1)
	v_pk_mul_f32 v[38:39], v[38:39], v[144:145]
	v_pk_mul_f32 v[48:49], v[48:49], v[138:139]
	v_pk_mul_f32 v[44:45], v[44:45], v[142:143]
	v_pk_mul_f32 v[40:41], v[40:41], v[146:147]
	s_waitcnt lgkmcnt(0)
	v_pk_mul_f32 v[36:37], v[36:37], v[150:151]
	v_pk_mul_f32 v[34:35], v[34:35], v[148:149]
	v_pk_mul_f32 v[62:63], v[62:63], v[136:137]
	v_pk_mul_f32 v[58:59], v[58:59], v[140:141]
	v_pk_mul_f32 v[54:55], v[54:55], v[144:145]
	v_pk_mul_f32 v[64:65], v[64:65], v[138:139]
	v_pk_mul_f32 v[60:61], v[60:61], v[142:143]
	v_pk_mul_f32 v[56:57], v[56:57], v[146:147]
	v_pk_mul_f32 v[52:53], v[52:53], v[150:151]
	v_pk_mul_f32 v[50:51], v[50:51], v[148:149]
	v_pk_mul_f32 v[30:31], v[30:31], v[136:137]
	v_pk_mul_f32 v[26:27], v[26:27], v[140:141]
	v_pk_mul_f32 v[22:23], v[22:23], v[144:145]
	v_pk_mul_f32 v[32:33], v[32:33], v[138:139]
	v_pk_mul_f32 v[28:29], v[28:29], v[142:143]
	v_pk_mul_f32 v[24:25], v[24:25], v[146:147]
	v_pk_mul_f32 v[20:21], v[20:21], v[150:151]
	v_pk_mul_f32 v[18:19], v[18:19], v[148:149]
	v_pk_mul_f32 v[78:79], v[78:79], v[136:137]
	v_pk_mul_f32 v[74:75], v[74:75], v[140:141]
	v_pk_mul_f32 v[70:71], v[70:71], v[144:145]
	v_pk_mul_f32 v[80:81], v[80:81], v[138:139]
	v_pk_mul_f32 v[76:77], v[76:77], v[142:143]
	v_pk_mul_f32 v[72:73], v[72:73], v[146:147]
	v_pk_mul_f32 v[68:69], v[68:69], v[150:151]
	v_pk_mul_f32 v[66:67], v[66:67], v[148:149]

; #define SBAR() __builtin_amdgcn_sched_barrier(0)
; #define VMW() asm volatile("s_waitcnt vmcnt(0)" ::: "memory")
; #define SWRITE_HV(bf) do { if constexpr (F8) { *(bf16x8*)(V_lds + (bf) * SHM_V + vws8) = S.st_v0; }                                                          \
;                            else { *(bf16x8*)(V_lds + (bf) * SHM_V + vst0) = S.st_v0; *(bf16x8*)(V_lds + (bf) * SHM_V + vst1) = S.st_v1; } } while (0)
; #define SWRITE_H(bf) do { SWRITE_HV(bf); SWRITE_HK(bf); } while (0)
; #define PSM(P0_, P1_, mn_, al_) partialSM<F8 ? 8 : 0, F8 ? 2 : 8, F8 ? 5 : 0>(P0_, P1_, m_reg, mn_, al_, dead_)
;     float pmax;
;     { float m0 = fmaxf(p0[0], p0[1]), m1 = fmaxf(p0[2], p0[3]), m2 = fmaxf(p1[0], p1[1]), m3 = fmaxf(p1[2], p1[3]);
; #pragma unroll
;       for (int r = 4; r < 16; r += 4) { m0 = fmaxf(fmaxf(m0, p0[r]), p0[r + 1]); m1 = fmaxf(fmaxf(m1, p0[r + 2]), p0[r + 3]); m2 = fmaxf(fmaxf(m2, p1[r]), p1[r + 1]); m3 = fmaxf(fmaxf(m3, p1[r + 2]), p1[r + 3]); }
;       pmax = fmaxf(fmaxf(m0, m1), fmaxf(m2, m3)); }
;     pmax = dead ? -__builtin_inff() : pmax;
;     { auto rr = __builtin_amdgcn_permlane32_swap(__float_as_uint(pmax), __float_as_uint(pmax), false, false);
;       pmax = fmaxf(__uint_as_float(rr[0]), __uint_as_float(rr[1])); }
;     constexpr float SCL = SCALE / (float)(1 << SH), C2 = 1.4426950408889634f * SCL;
;     if (__builtin_expect(__all((pmax - m_reg) * SCL <= (float)THRI), 1)) { mn = m_reg; alpha = 1.f; }
;     else { mn = fmaxf(m_reg, pmax); alpha = __builtin_amdgcn_exp2f((m_reg - mn) * C2); m_reg = mn; }
;     const float mnL = dead ? -__builtin_inff() : -mn * C2 + (float)PSH;
;     for (int r = 0; r < 16; ++r) p0[r] = fmaf(p0[r], C2, mnL); for (int r = 0; r < 16; ++r) p1[r] = fmaf(p1[r], C2, mnL);
; template <class Epi, bool F8 = false>
; __device__ __forceinline__ void block(const BlockRef& cur, int skv, char* lds, Seam& S, bool moba, unsigned selmask, const Epi& E) {
;     ...
;     f32x16 pA0, pA1, pB0, pB1; float mnA, mnB, alA, alB; bf16x8 pa0, pa1, pa2, pa3;
;     SWRITE_HV(0); SBAR();
;     if (NT > 1) SLOAD_H(Kh, Vh, KBASE(1));
;     SBAR(); QKT(0, pA0, pA1);
;     MASKT(pA0, pA1, 0); PSM(pA0, pA1, mnA, alA);
;     if (NT > 1) { VMW(); SWRITE_H(1); }
;     __syncthreads();
.LBB0_1053:
	s_cmp_lt_u32 s86, s72
	s_cselect_b64 s[6:7], -1, 0
	s_lshr_b32 s8, s81, 2
	s_lshl_b32 s8, 1, s8
	v_and_b32_e32 v12, s8, v131
	v_cmp_eq_u32_e32 vcc, 0, v12
	v_max_f32_e32 v12, v98, v99
	v_max_f32_e32 v13, v100, v101
	v_max_f32_e32 v136, v84, v85
	v_max3_f32 v137, v82, v83, v86
	v_max3_f32 v136, v136, v88, v89
	v_max3_f32 v12, v12, v102, v103
	v_max3_f32 v13, v13, v104, v105
	v_max3_f32 v137, v137, v87, v90
	v_max3_f32 v136, v136, v92, v93
	v_max3_f32 v12, v12, v106, v107
	v_max3_f32 v13, v13, v108, v109
	v_max3_f32 v137, v137, v91, v94
	v_max3_f32 v136, v136, v96, v97
	v_max3_f32 v12, v12, v110, v111
	v_max3_f32 v13, v13, v112, v113
	v_max3_f32 v136, v137, v95, v136
	v_max3_f32 v12, v12, v13, v136
	s_and_b64 s[6:7], s[6:7], vcc
	v_cndmask_b32_e64 v12, v12, v210, s[6:7]
	v_mov_b32_e32 v13, v12
	s_nop 1
	v_permlane32_swap_b32_e32 v12, v13
	v_max_f32_e32 v12, v12, v13
	v_sub_f32_e32 v13, v12, v16
	v_mul_f32_e32 v13, 0x39b504f3, v13
	v_cmp_ge_f32_e32 vcc, 2.0, v13
	s_cmp_eq_u64 vcc, exec
	s_cselect_b64 s[8:9], -1, 0
	s_andn2_b64 vcc, exec, s[70:71]
	s_barrier
	s_cbranch_vccnz .LBB0_1055
	s_waitcnt vmcnt(0)
	s_waitcnt vmcnt(1)
	ds_write_b128 v160, v[4:7] offset:16384
	s_waitcnt vmcnt(0)
	ds_write_b128 v161, v[8:11] offset:49152
.LBB0_1055:
	s_waitcnt vmcnt(1)
	v_max_f32_e32 v5, v16, v12
	v_sub_f32_e32 v4, v16, v5
	v_mul_f32_e32 v4, 0x3a0293ee, v4
	v_exp_f32_e32 v4, v4
	s_nop 0
	v_cndmask_b32_e64 v4, v4, 1.0, s[8:9]
	v_cmp_gt_f32_e32 vcc, 1.0, v4
	s_cbranch_vccz .LBB0_1059
	s_and_saveexec_b64 s[10:11], s[4:5]
	ds_write_b32 v155, v4 offset:128
	s_or_b64 exec, exec, s[10:11]
	s_waitcnt lgkmcnt(0)
	v_add_u32_e32 v140, s73, v154
	s_waitcnt vmcnt(0)
	ds_read_b128 v[6:9], v140 offset:224
	ds_read_b128 v[10:13], v140 offset:192
	ds_read_b128 v[136:139], v140 offset:160
	ds_read_b128 v[140:143], v140 offset:128
	s_waitcnt lgkmcnt(3)
	v_pk_mul_f32 v[46:47], v[46:47], v[6:7]
	s_waitcnt lgkmcnt(2)
	v_pk_mul_f32 v[42:43], v[42:43], v[10:11]
	s_waitcnt lgkmcnt(1)
	v_pk_mul_f32 v[38:39], v[38:39], v[136:137]
	v_pk_mul_f32 v[48:49], v[48:49], v[8:9]
	v_pk_mul_f32 v[44:45], v[44:45], v[12:13]
	v_pk_mul_f32 v[40:41], v[40:41], v[138:139]
	s_waitcnt lgkmcnt(0)
	v_pk_mul_f32 v[36:37], v[36:37], v[142:143]
	v_pk_mul_f32 v[34:35], v[34:35], v[140:141]
	v_pk_mul_f32 v[62:63], v[62:63], v[6:7]
	v_pk_mul_f32 v[58:59], v[58:59], v[10:11]
	v_pk_mul_f32 v[54:55], v[54:55], v[136:137]
	v_pk_mul_f32 v[64:65], v[64:65], v[8:9]
	v_pk_mul_f32 v[60:61], v[60:61], v[12:13]
	v_pk_mul_f32 v[56:57], v[56:57], v[138:139]
	v_pk_mul_f32 v[52:53], v[52:53], v[142:143]
	v_pk_mul_f32 v[50:51], v[50:51], v[140:141]
	v_pk_mul_f32 v[30:31], v[30:31], v[6:7]
	v_pk_mul_f32 v[26:27], v[26:27], v[10:11]
	v_pk_mul_f32 v[22:23], v[22:23], v[136:137]
	v_pk_mul_f32 v[32:33], v[32:33], v[8:9]
	v_pk_mul_f32 v[28:29], v[28:29], v[12:13]
	v_pk_mul_f32 v[24:25], v[24:25], v[138:139]
	v_pk_mul_f32 v[20:21], v[20:21], v[142:143]
	v_pk_mul_f32 v[18:19], v[18:19], v[140:141]
	v_pk_mul_f32 v[78:79], v[78:79], v[6:7]
	v_pk_mul_f32 v[74:75], v[74:75], v[10:11]
	v_pk_mul_f32 v[70:71], v[70:71], v[136:137]
	v_pk_mul_f32 v[80:81], v[80:81], v[8:9]
	v_pk_mul_f32 v[76:77], v[76:77], v[12:13]
	v_pk_mul_f32 v[72:73], v[72:73], v[138:139]
	v_pk_mul_f32 v[68:69], v[68:69], v[142:143]
	v_pk_mul_f32 v[66:67], v[66:67], v[140:141]

; __device__ __forceinline__ void finishSM8(f32x16& p0, f32x16& p1, float alpha, float& l_reg, i32x8& pa) {
;     for (int r = 0; r < 16; ++r) p1[r] = __builtin_amdgcn_exp2f(p1[r]);
;     float ps;
;     { float s0 = p0[0] + p0[1], s1 = p0[2] + p0[3], s2 = p1[0] + p1[1], s3 = p1[2] + p1[3];
; #pragma unroll
;       for (int r = 4; r < 16; r += 4) { s0 += p0[r]; s0 += p0[r + 1]; s1 += p0[r + 2]; s1 += p0[r + 3]; s2 += p1[r]; s2 += p1[r + 1]; s3 += p1[r + 2]; s3 += p1[r + 3]; }
;       ps = (s0 + s1) + (s2 + s3); }
;     { auto rr = __builtin_amdgcn_permlane32_swap(__float_as_uint(ps), __float_as_uint(ps), false, false);
;       ps = __uint_as_float(rr[0]) + __uint_as_float(rr[1]); }
;     l_reg = l_reg * alpha + ps;
; #pragma unroll
;     for (int d = 0; d < 4; ++d) { int w0 = 0, w1 = 0;
;         w0 = __builtin_amdgcn_cvt_pk_fp8_f32(p0[4 * d], p0[4 * d + 1], w0, false); w0 = __builtin_amdgcn_cvt_pk_fp8_f32(p0[4 * d + 2], p0[4 * d + 3], w0, true);
;         w1 = __builtin_amdgcn_cvt_pk_fp8_f32(p1[4 * d], p1[4 * d + 1], w1, false); w1 = __builtin_amdgcn_cvt_pk_fp8_f32(p1[4 * d + 2], p1[4 * d + 3], w1, true);
;         pa[d] = w0; pa[4 + d] = w1; }
.LBB0_1205:
	s_barrier
	v_add_f32_e32 v146, v147, v150
	v_add_f32_e32 v166, v10, v12
	v_add_f32_e32 v167, v151, v165
	v_add_f32_e32 v168, v152, v160
	v_add_f32_e32 v146, v148, v146
	v_add_f32_e32 v166, v14, v166
	v_add_f32_e32 v167, v163, v167
	v_add_f32_e32 v168, v161, v168
	v_add_f32_e32 v146, v149, v146
	v_add_f32_e32 v166, v15, v166
	v_add_f32_e32 v167, v164, v167
	v_add_f32_e32 v168, v162, v168
	v_add_f32_e32 v146, v11, v146
	v_add_f32_e32 v166, v4, v166
	v_add_f32_e32 v167, v153, v167
	v_add_f32_e32 v168, v17, v168
	v_add_f32_e32 v146, v13, v146
	v_add_f32_e32 v166, v5, v166
	v_add_f32_e32 v167, v159, v167
	v_add_f32_e32 v168, v154, v168
	v_add_f32_e32 v146, v8, v146
	v_add_f32_e32 v166, v6, v166
	v_add_f32_e32 v167, v157, v167
	v_add_f32_e32 v168, v155, v168
	v_add_f32_e32 v146, v9, v146
	v_add_f32_e32 v166, v7, v166
	v_add_f32_e32 v167, v158, v167
	v_add_f32_e32 v168, v156, v168
	v_add_f32_e32 v146, v166, v146
	v_add_f32_e32 v166, v167, v168
	v_add_f32_e32 v166, v166, v146
	v_mov_b32_e32 v167, v166
	s_nop 1
	v_permlane32_swap_b32_e32 v166, v167
	v_cvt_pk_fp8_f32 v146, v147, v150
	v_cvt_pk_fp8_f32 v150, v151, v165
	v_cvt_pk_fp8_f32 v147, v148, v149
	v_cvt_pk_fp8_f32 v150, v152, v160 op_sel:[0,0,1]
	v_cvt_pk_fp8_f32 v152, v153, v159
	v_cvt_pk_fp8_f32 v151, v163, v164
	v_cvt_pk_fp8_f32 v148, v11, v13
	v_cvt_pk_fp8_f32 v149, v8, v9
	v_cvt_pk_fp8_f32 v153, v157, v158
	v_cvt_pk_fp8_f32 v146, v10, v12 op_sel:[0,0,1]
	v_cvt_pk_fp8_f32 v147, v14, v15 op_sel:[0,0,1]
	v_cvt_pk_fp8_f32 v151, v161, v162 op_sel:[0,0,1]
	v_cvt_pk_fp8_f32 v148, v4, v5 op_sel:[0,0,1]
	v_cvt_pk_fp8_f32 v152, v17, v154 op_sel:[0,0,1]
	v_cvt_pk_fp8_f32 v149, v6, v7 op_sel:[0,0,1]
	v_cvt_pk_fp8_f32 v153, v155, v156 op_sel:[0,0,1]
	v_add_f32_e32 v4, v242, v243
	v_fmac_f32_e32 v4, v215, v2
	v_add_f32_e32 v215, v166, v167
	s_add_u32 s90, s90, 0x4000
	v_fmac_f32_e32 v215, v4, v16
	s_addc_u32 s91, s91, 0
	s_add_i32 s73, s73, 2
	v_add_u32_e32 v240, 0xffffff80, v240
	s_addk_i32 s78, 0x80
	s_and_b64 vcc, exec, s[70:71]
	s_cbranch_vccnz .LBB0_1245

;     float pmax;
;     { float m0 = fmaxf(p0[0], p0[1]), m1 = fmaxf(p0[2], p0[3]), m2 = fmaxf(p1[0], p1[1]), m3 = fmaxf(p1[2], p1[3]);
; #pragma unroll
;       for (int r = 4; r < 16; r += 4) { m0 = fmaxf(fmaxf(m0, p0[r]), p0[r + 1]); m1 = fmaxf(fmaxf(m1, p0[r + 2]), p0[r + 3]); m2 = fmaxf(fmaxf(m2, p1[r]), p1[r + 1]); m3 = fmaxf(fmaxf(m3, p1[r + 2]), p1[r + 3]); }
;       pmax = fmaxf(fmaxf(m0, m1), fmaxf(m2, m3)); }
;     pmax = dead ? -__builtin_inff() : pmax;
;     { auto rr = __builtin_amdgcn_permlane32_swap(__float_as_uint(pmax), __float_as_uint(pmax), false, false);
;       pmax = fmaxf(__uint_as_float(rr[0]), __uint_as_float(rr[1])); }
;     constexpr float SCL = SCALE / (float)(1 << SH), C2 = 1.4426950408889634f * SCL;
;     if (__builtin_expect(__all((pmax - m_reg) * SCL <= (float)THRI), 1)) { mn = m_reg; alpha = 1.f; }
;     else { mn = fmaxf(m_reg, pmax); alpha = __builtin_amdgcn_exp2f((m_reg - mn) * C2); m_reg = mn; }
;     const float mnL = dead ? -__builtin_inff() : -mn * C2 + (float)PSH;
;     for (int r = 0; r < 16; ++r) p0[r] = fmaf(p0[r], C2, mnL); for (int r = 0; r < 16; ++r) p1[r] = fmaf(p1[r], C2, mnL);
.LBB0_1215:
	v_max_f32_e32 v2, v162, v163
	v_max_f32_e32 v4, v164, v165
	v_max_f32_e32 v5, v148, v149
	v_max3_f32 v6, v146, v147, v150
	v_max3_f32 v5, v5, v152, v153
	v_max3_f32 v2, v2, v166, v167
	v_max3_f32 v4, v4, v168, v169
	v_max3_f32 v6, v6, v151, v154
	v_max3_f32 v5, v5, v156, v157
	v_max3_f32 v2, v2, v170, v171
	v_max3_f32 v4, v4, v172, v173
	v_max3_f32 v6, v6, v155, v158
	v_max3_f32 v5, v5, v160, v161
	v_max3_f32 v2, v2, v174, v175
	v_max3_f32 v4, v4, v176, v177
	v_max3_f32 v5, v6, v159, v5
	v_max3_f32 v2, v2, v4, v5
	v_mov_b32_e32 v4, v2
	s_nop 1
	v_permlane32_swap_b32_e32 v2, v4
	v_max_f32_e32 v2, v2, v4
	v_max_f32_e32 v5, v241, v241
	v_max_f32_e32 v242, v5, v2
	v_sub_f32_e32 v4, v2, v241
	v_sub_f32_e32 v2, v241, v242
	v_mul_f32_e32 v2, 0x3a0293ee, v2
	v_mul_f32_e32 v4, 0x39b504f3, v4
	v_exp_f32_e32 v2, v2
	v_cmp_ge_f32_e32 vcc, 2.0, v4
	s_cmp_eq_u64 vcc, exec
	s_cselect_b64 s[6:7], -1, 0
	v_cndmask_b32_e64 v2, v2, 1.0, s[6:7]
	v_cmp_gt_f32_e32 vcc, 1.0, v2
	s_cbranch_vccz .LBB0_1219
	s_and_saveexec_b64 s[8:9], s[4:5]
	ds_write_b32 v238, v2 offset:128
	s_or_b64 exec, exec, s[8:9]
	s_waitcnt lgkmcnt(0)
	v_add_u32_e32 v4, s93, v239
	ds_read_b128 v[194:197], v4 offset:224
	ds_read_b128 v[12:15], v4 offset:192
	ds_read_b128 v[8:11], v4 offset:160
	ds_read_b128 v[4:7], v4 offset:128
	s_waitcnt lgkmcnt(0)
	v_pk_mul_f32 v[142:143], v[142:143], v[194:195]
	v_pk_mul_f32 v[138:139], v[138:139], v[12:13]
	v_pk_mul_f32 v[134:135], v[134:135], v[8:9]
	v_pk_mul_f32 v[144:145], v[144:145], v[196:197]
	v_pk_mul_f32 v[140:141], v[140:141], v[14:15]
	v_pk_mul_f32 v[136:137], v[136:137], v[10:11]
	v_pk_mul_f32 v[132:133], v[132:133], v[6:7]
	v_pk_mul_f32 v[130:131], v[130:131], v[4:5]
	v_pk_mul_f32 v[126:127], v[126:127], v[194:195]
	v_pk_mul_f32 v[122:123], v[122:123], v[12:13]
	v_pk_mul_f32 v[118:119], v[118:119], v[8:9]
	v_pk_mul_f32 v[128:129], v[128:129], v[196:197]
	v_pk_mul_f32 v[124:125], v[124:125], v[14:15]
	v_pk_mul_f32 v[120:121], v[120:121], v[10:11]
	v_pk_mul_f32 v[116:117], v[116:117], v[6:7]
	v_pk_mul_f32 v[114:115], v[114:115], v[4:5]
	v_pk_mul_f32 v[110:111], v[110:111], v[194:195]
	v_pk_mul_f32 v[106:107], v[106:107], v[12:13]
	v_pk_mul_f32 v[102:103], v[102:103], v[8:9]
	v_pk_mul_f32 v[112:113], v[112:113], v[196:197]
	v_pk_mul_f32 v[108:109], v[108:109], v[14:15]
	v_pk_mul_f32 v[104:105], v[104:105], v[10:11]
	v_pk_mul_f32 v[100:101], v[100:101], v[6:7]
	v_pk_mul_f32 v[98:99], v[98:99], v[4:5]
	v_pk_mul_f32 v[94:95], v[94:95], v[194:195]
	v_pk_mul_f32 v[90:91], v[90:91], v[12:13]
	v_pk_mul_f32 v[86:87], v[86:87], v[8:9]
	v_pk_mul_f32 v[96:97], v[96:97], v[196:197]
	v_pk_mul_f32 v[92:93], v[92:93], v[14:15]
	v_pk_mul_f32 v[88:89], v[88:89], v[10:11]
	v_pk_mul_f32 v[84:85], v[84:85], v[6:7]
	v_pk_mul_f32 v[82:83], v[82:83], v[4:5]
	v_pk_mul_f32 v[78:79], v[78:79], v[194:195]
	v_pk_mul_f32 v[74:75], v[74:75], v[12:13]
	v_pk_mul_f32 v[70:71], v[70:71], v[8:9]
	v_pk_mul_f32 v[80:81], v[80:81], v[196:197]
	v_pk_mul_f32 v[76:77], v[76:77], v[14:15]
	v_pk_mul_f32 v[72:73], v[72:73], v[10:11]
	v_pk_mul_f32 v[68:69], v[68:69], v[6:7]
	v_pk_mul_f32 v[66:67], v[66:67], v[4:5]
	v_pk_mul_f32 v[62:63], v[62:63], v[194:195]
	v_pk_mul_f32 v[58:59], v[58:59], v[12:13]
	v_pk_mul_f32 v[54:55], v[54:55], v[8:9]
	v_pk_mul_f32 v[64:65], v[64:65], v[196:197]
	v_pk_mul_f32 v[60:61], v[60:61], v[14:15]
	v_pk_mul_f32 v[56:57], v[56:57], v[10:11]
	v_pk_mul_f32 v[52:53], v[52:53], v[6:7]
	v_pk_mul_f32 v[50:51], v[50:51], v[4:5]
	v_pk_mul_f32 v[46:47], v[46:47], v[194:195]
	v_pk_mul_f32 v[42:43], v[42:43], v[12:13]
	v_pk_mul_f32 v[38:39], v[38:39], v[8:9]
	v_pk_mul_f32 v[48:49], v[48:49], v[196:197]
	v_pk_mul_f32 v[44:45], v[44:45], v[14:15]
	v_pk_mul_f32 v[40:41], v[40:41], v[10:11]
	v_pk_mul_f32 v[36:37], v[36:37], v[6:7]
	v_pk_mul_f32 v[34:35], v[34:35], v[4:5]
	v_pk_mul_f32 v[30:31], v[30:31], v[194:195]
	v_pk_mul_f32 v[26:27], v[26:27], v[12:13]
	v_pk_mul_f32 v[22:23], v[22:23], v[8:9]
	v_pk_mul_f32 v[32:33], v[32:33], v[196:197]
	v_pk_mul_f32 v[28:29], v[28:29], v[14:15]
	v_pk_mul_f32 v[24:25], v[24:25], v[10:11]
	v_pk_mul_f32 v[20:21], v[20:21], v[6:7]
	v_pk_mul_f32 v[18:19], v[18:19], v[4:5]

; __device__ __forceinline__ void finishSM8(f32x16& p0, f32x16& p1, float alpha, float& l_reg, i32x8& pa) {
;     for (int r = 0; r < 16; ++r) p1[r] = __builtin_amdgcn_exp2f(p1[r]);
;     float ps;
;     { float s0 = p0[0] + p0[1], s1 = p0[2] + p0[3], s2 = p1[0] + p1[1], s3 = p1[2] + p1[3];
; #pragma unroll
;       for (int r = 4; r < 16; r += 4) { s0 += p0[r]; s0 += p0[r + 1]; s1 += p0[r + 2]; s1 += p0[r + 3]; s2 += p1[r]; s2 += p1[r + 1]; s3 += p1[r + 2]; s3 += p1[r + 3]; }
;       ps = (s0 + s1) + (s2 + s3); }
;     { auto rr = __builtin_amdgcn_permlane32_swap(__float_as_uint(ps), __float_as_uint(ps), false, false);
;       ps = __uint_as_float(rr[0]) + __uint_as_float(rr[1]); }
;     l_reg = l_reg * alpha + ps;
; #pragma unroll
;     for (int d = 0; d < 4; ++d) { int w0 = 0, w1 = 0;
;         w0 = __builtin_amdgcn_cvt_pk_fp8_f32(p0[4 * d], p0[4 * d + 1], w0, false); w0 = __builtin_amdgcn_cvt_pk_fp8_f32(p0[4 * d + 2], p0[4 * d + 3], w0, true);
;         w1 = __builtin_amdgcn_cvt_pk_fp8_f32(p1[4 * d], p1[4 * d + 1], w1, false); w1 = __builtin_amdgcn_cvt_pk_fp8_f32(p1[4 * d + 2], p1[4 * d + 3], w1, true);
;         pa[d] = w0; pa[4 + d] = w1; }
.LBB0_1225:
	v_add_f32_e32 v166, v154, v155
	v_add_f32_e32 v167, v10, v12
	v_add_f32_e32 v168, v164, v165
	v_add_f32_e32 v169, v158, v159
	v_add_f32_e32 v166, v150, v166
	v_add_f32_e32 v167, v14, v167
	v_add_f32_e32 v168, v162, v168
	v_add_f32_e32 v169, v160, v169
	v_add_f32_e32 v166, v151, v166
	v_add_f32_e32 v167, v15, v167
	v_add_f32_e32 v168, v163, v168
	v_add_f32_e32 v169, v161, v169
	v_add_f32_e32 v166, v11, v166
	v_add_f32_e32 v167, v4, v167
	v_add_f32_e32 v168, v156, v168
	v_add_f32_e32 v169, v146, v169
	v_add_f32_e32 v166, v13, v166
	v_add_f32_e32 v167, v5, v167
	v_add_f32_e32 v168, v157, v168
	v_add_f32_e32 v169, v147, v169
	v_add_f32_e32 v166, v8, v166
	v_add_f32_e32 v167, v6, v167
	v_add_f32_e32 v168, v152, v168
	v_add_f32_e32 v169, v148, v169
	v_add_f32_e32 v166, v9, v166
	v_add_f32_e32 v167, v7, v167
	v_add_f32_e32 v168, v153, v168
	v_add_f32_e32 v169, v149, v169
	v_add_f32_e32 v166, v167, v166
	v_add_f32_e32 v167, v168, v169
	v_add_f32_e32 v242, v167, v166
	v_mov_b32_e32 v243, v242
	s_nop 1
	v_permlane32_swap_b32_e32 v242, v243
	v_cvt_pk_fp8_f32 v166, v154, v155
	v_cvt_pk_fp8_f32 v170, v164, v165
	v_cvt_pk_fp8_f32 v167, v150, v151
	v_cvt_pk_fp8_f32 v171, v162, v163
	v_cvt_pk_fp8_f32 v168, v11, v13
	v_cvt_pk_fp8_f32 v172, v156, v157
	v_cvt_pk_fp8_f32 v169, v8, v9
	v_cvt_pk_fp8_f32 v173, v152, v153
	v_cvt_pk_fp8_f32 v166, v10, v12 op_sel:[0,0,1]
	v_cvt_pk_fp8_f32 v170, v158, v159 op_sel:[0,0,1]
	v_cvt_pk_fp8_f32 v167, v14, v15 op_sel:[0,0,1]
	v_cvt_pk_fp8_f32 v171, v160, v161 op_sel:[0,0,1]
	v_cvt_pk_fp8_f32 v168, v4, v5 op_sel:[0,0,1]
	v_cvt_pk_fp8_f32 v172, v146, v147 op_sel:[0,0,1]
	v_cvt_pk_fp8_f32 v169, v6, v7 op_sel:[0,0,1]
	v_cvt_pk_fp8_f32 v173, v148, v149 op_sel:[0,0,1]
	ds_read_b128 v[4:7], v203
	ds_read_b128 v[146:149], v203 offset:2048
	ds_read_b128 v[8:11], v214
	ds_read_b128 v[150:153], v214 offset:2048
	s_waitcnt lgkmcnt(0)
	v_mfma_f32_32x32x64_f8f6f4 v[130:145], v[166:173], v[4:11], v[130:145]
	ds_read_b128 v[4:7], v203 offset:4096
	ds_read_b128 v[8:11], v214 offset:4096
	v_mfma_f32_32x32x64_f8f6f4 v[114:129], v[166:173], v[146:153], v[114:129]
	ds_read_b128 v[146:149], v203 offset:6144
	ds_read_b128 v[150:153], v214 offset:6144
	s_waitcnt lgkmcnt(0)
	v_mfma_f32_32x32x64_f8f6f4 v[98:113], v[166:173], v[4:11], v[98:113]
	ds_read_b128 v[4:7], v203 offset:16384
	ds_read_b128 v[8:11], v214 offset:16384
	v_mfma_f32_32x32x64_f8f6f4 v[82:97], v[166:173], v[146:153], v[82:97]
	ds_read_b128 v[146:149], v203 offset:18432
	ds_read_b128 v[150:153], v214 offset:18432
	s_waitcnt lgkmcnt(0)
	v_mfma_f32_32x32x64_f8f6f4 v[66:81], v[166:173], v[4:11], v[66:81]
	ds_read_b128 v[4:7], v203 offset:20480
	ds_read_b128 v[8:11], v214 offset:20480
	v_mfma_f32_32x32x64_f8f6f4 v[50:65], v[166:173], v[146:153], v[50:65]
	ds_read_b128 v[146:149], v203 offset:22528
	ds_read_b128 v[150:153], v214 offset:22528
	s_waitcnt lgkmcnt(0)
	v_mfma_f32_32x32x64_f8f6f4 v[34:49], v[166:173], v[4:11], v[34:49]
	v_mfma_f32_32x32x64_f8f6f4 v[18:33], v[166:173], v[146:153], v[18:33]
	s_nop 15
	s_nop 15
	s_mov_b64 s[8:9], -1
	s_and_b64 vcc, exec, s[70:71]
	s_cbranch_vccz .LBB0_1227
	s_waitcnt vmcnt(0) lgkmcnt(0)
	s_mov_b64 s[8:9], 0

;     float pmax;
;     { float m0 = fmaxf(p0[0], p0[1]), m1 = fmaxf(p0[2], p0[3]), m2 = fmaxf(p1[0], p1[1]), m3 = fmaxf(p1[2], p1[3]);
; #pragma unroll
;       for (int r = 4; r < 16; r += 4) { m0 = fmaxf(fmaxf(m0, p0[r]), p0[r + 1]); m1 = fmaxf(fmaxf(m1, p0[r + 2]), p0[r + 3]); m2 = fmaxf(fmaxf(m2, p1[r]), p1[r + 1]); m3 = fmaxf(fmaxf(m3, p1[r + 2]), p1[r + 3]); }
;       pmax = fmaxf(fmaxf(m0, m1), fmaxf(m2, m3)); }
;     pmax = dead ? -__builtin_inff() : pmax;
;     { auto rr = __builtin_amdgcn_permlane32_swap(__float_as_uint(pmax), __float_as_uint(pmax), false, false);
;       pmax = fmaxf(__uint_as_float(rr[0]), __uint_as_float(rr[1])); }
;     constexpr float SCL = SCALE / (float)(1 << SH), C2 = 1.4426950408889634f * SCL;
;     if (__builtin_expect(__all((pmax - m_reg) * SCL <= (float)THRI), 1)) { mn = m_reg; alpha = 1.f; }
;     else { mn = fmaxf(m_reg, pmax); alpha = __builtin_amdgcn_exp2f((m_reg - mn) * C2); m_reg = mn; }
;     const float mnL = dead ? -__builtin_inff() : -mn * C2 + (float)PSH;
;     for (int r = 0; r < 16; ++r) p0[r] = fmaf(p0[r], C2, mnL); for (int r = 0; r < 16; ++r) p1[r] = fmaf(p1[r], C2, mnL);
.LBB0_1233:
	v_max_f32_e32 v4, v162, v163
	v_max_f32_e32 v5, v164, v165
	v_max_f32_e32 v6, v148, v149
	v_max3_f32 v7, v146, v147, v150
	v_max3_f32 v6, v6, v152, v153
	v_max3_f32 v4, v4, v166, v167
	v_max3_f32 v5, v5, v168, v169
	v_max3_f32 v7, v7, v151, v154
	v_max3_f32 v6, v6, v156, v157
	v_max3_f32 v4, v4, v170, v171
	v_max3_f32 v5, v5, v172, v173
	v_max3_f32 v7, v7, v155, v158
	v_max3_f32 v6, v6, v160, v161
	v_max3_f32 v4, v4, v174, v175
	v_max3_f32 v5, v5, v176, v177
	v_max3_f32 v6, v7, v159, v6
	v_max3_f32 v4, v4, v5, v6
	v_mov_b32_e32 v5, v4
	s_nop 1
	v_permlane32_swap_b32_e32 v4, v5
	v_max_f32_e32 v4, v4, v5
	v_max_f32_e32 v6, v241, v241
	v_max_f32_e32 v17, v6, v4
	v_sub_f32_e32 v5, v4, v241
	v_sub_f32_e32 v4, v241, v17
	v_mul_f32_e32 v4, 0x3a0293ee, v4
	v_mul_f32_e32 v5, 0x39b504f3, v5
	v_exp_f32_e32 v4, v4
	v_cmp_ge_f32_e32 vcc, 2.0, v5
	s_cmp_eq_u64 vcc, exec
	s_cselect_b64 s[6:7], -1, 0
	v_readlane_b32 s66, v253, 52
	v_cndmask_b32_e64 v16, v4, 1.0, s[6:7]
	v_readlane_b32 s67, v253, 53
	v_cmp_gt_f32_e32 vcc, 1.0, v16
	s_cbranch_vccz .LBB0_1237
	s_and_saveexec_b64 s[8:9], s[4:5]
	ds_write_b32 v238, v16 offset:128
	s_or_b64 exec, exec, s[8:9]
	s_waitcnt lgkmcnt(0)
	v_add_u32_e32 v4, s93, v239
	ds_read_b128 v[194:197], v4 offset:224
	ds_read_b128 v[12:15], v4 offset:192
	ds_read_b128 v[8:11], v4 offset:160
	ds_read_b128 v[4:7], v4 offset:128
	s_waitcnt lgkmcnt(0)
	v_pk_mul_f32 v[142:143], v[142:143], v[194:195]
	v_pk_mul_f32 v[138:139], v[138:139], v[12:13]
	v_pk_mul_f32 v[134:135], v[134:135], v[8:9]
	v_pk_mul_f32 v[144:145], v[144:145], v[196:197]
	v_pk_mul_f32 v[140:141], v[140:141], v[14:15]
	v_pk_mul_f32 v[136:137], v[136:137], v[10:11]
	v_pk_mul_f32 v[132:133], v[132:133], v[6:7]
	v_pk_mul_f32 v[130:131], v[130:131], v[4:5]
	v_pk_mul_f32 v[126:127], v[126:127], v[194:195]
	v_pk_mul_f32 v[122:123], v[122:123], v[12:13]
	v_pk_mul_f32 v[118:119], v[118:119], v[8:9]
	v_pk_mul_f32 v[128:129], v[128:129], v[196:197]
	v_pk_mul_f32 v[124:125], v[124:125], v[14:15]
	v_pk_mul_f32 v[120:121], v[120:121], v[10:11]
	v_pk_mul_f32 v[116:117], v[116:117], v[6:7]
	v_pk_mul_f32 v[114:115], v[114:115], v[4:5]
	v_pk_mul_f32 v[110:111], v[110:111], v[194:195]
	v_pk_mul_f32 v[106:107], v[106:107], v[12:13]
	v_pk_mul_f32 v[102:103], v[102:103], v[8:9]
	v_pk_mul_f32 v[112:113], v[112:113], v[196:197]
	v_pk_mul_f32 v[108:109], v[108:109], v[14:15]
	v_pk_mul_f32 v[104:105], v[104:105], v[10:11]
	v_pk_mul_f32 v[100:101], v[100:101], v[6:7]
	v_pk_mul_f32 v[98:99], v[98:99], v[4:5]
	v_pk_mul_f32 v[94:95], v[94:95], v[194:195]
	v_pk_mul_f32 v[90:91], v[90:91], v[12:13]
	v_pk_mul_f32 v[86:87], v[86:87], v[8:9]
	v_pk_mul_f32 v[96:97], v[96:97], v[196:197]
	v_pk_mul_f32 v[92:93], v[92:93], v[14:15]
	v_pk_mul_f32 v[88:89], v[88:89], v[10:11]
	v_pk_mul_f32 v[84:85], v[84:85], v[6:7]
	v_pk_mul_f32 v[82:83], v[82:83], v[4:5]
	v_pk_mul_f32 v[78:79], v[78:79], v[194:195]
	v_pk_mul_f32 v[74:75], v[74:75], v[12:13]
	v_pk_mul_f32 v[70:71], v[70:71], v[8:9]
	v_pk_mul_f32 v[80:81], v[80:81], v[196:197]
	v_pk_mul_f32 v[76:77], v[76:77], v[14:15]
	v_pk_mul_f32 v[72:73], v[72:73], v[10:11]
	v_pk_mul_f32 v[68:69], v[68:69], v[6:7]
	v_pk_mul_f32 v[66:67], v[66:67], v[4:5]
	v_pk_mul_f32 v[62:63], v[62:63], v[194:195]
	v_pk_mul_f32 v[58:59], v[58:59], v[12:13]
	v_pk_mul_f32 v[54:55], v[54:55], v[8:9]
	v_pk_mul_f32 v[64:65], v[64:65], v[196:197]
	v_pk_mul_f32 v[60:61], v[60:61], v[14:15]
	v_pk_mul_f32 v[56:57], v[56:57], v[10:11]
	v_pk_mul_f32 v[52:53], v[52:53], v[6:7]
	v_pk_mul_f32 v[50:51], v[50:51], v[4:5]
	v_pk_mul_f32 v[46:47], v[46:47], v[194:195]
	v_pk_mul_f32 v[42:43], v[42:43], v[12:13]
	v_pk_mul_f32 v[38:39], v[38:39], v[8:9]
	v_pk_mul_f32 v[48:49], v[48:49], v[196:197]
	v_pk_mul_f32 v[44:45], v[44:45], v[14:15]
	v_pk_mul_f32 v[40:41], v[40:41], v[10:11]
	v_pk_mul_f32 v[36:37], v[36:37], v[6:7]
	v_pk_mul_f32 v[34:35], v[34:35], v[4:5]
	v_pk_mul_f32 v[30:31], v[30:31], v[194:195]
	v_pk_mul_f32 v[26:27], v[26:27], v[12:13]
	v_pk_mul_f32 v[22:23], v[22:23], v[8:9]
	v_pk_mul_f32 v[32:33], v[32:33], v[196:197]
	v_pk_mul_f32 v[28:29], v[28:29], v[14:15]
	v_pk_mul_f32 v[24:25], v[24:25], v[10:11]
	v_pk_mul_f32 v[20:21], v[20:21], v[6:7]
	v_pk_mul_f32 v[18:19], v[18:19], v[4:5]

;     float pmax;
;     { float m0 = fmaxf(p0[0], p0[1]), m1 = fmaxf(p0[2], p0[3]), m2 = fmaxf(p1[0], p1[1]), m3 = fmaxf(p1[2], p1[3]);
; #pragma unroll
;       for (int r = 4; r < 16; r += 4) { m0 = fmaxf(fmaxf(m0, p0[r]), p0[r + 1]); m1 = fmaxf(fmaxf(m1, p0[r + 2]), p0[r + 3]); m2 = fmaxf(fmaxf(m2, p1[r]), p1[r + 1]); m3 = fmaxf(fmaxf(m3, p1[r + 2]), p1[r + 3]); }
;       pmax = fmaxf(fmaxf(m0, m1), fmaxf(m2, m3)); }
;     pmax = dead ? -__builtin_inff() : pmax;
;     { auto rr = __builtin_amdgcn_permlane32_swap(__float_as_uint(pmax), __float_as_uint(pmax), false, false);
;       pmax = fmaxf(__uint_as_float(rr[0]), __uint_as_float(rr[1])); }
;     constexpr float SCL = SCALE / (float)(1 << SH), C2 = 1.4426950408889634f * SCL;
;     if (__builtin_expect(__all((pmax - m_reg) * SCL <= (float)THRI), 1)) { mn = m_reg; alpha = 1.f; }
;     else { mn = fmaxf(m_reg, pmax); alpha = __builtin_amdgcn_exp2f((m_reg - mn) * C2); m_reg = mn; }
;     const float mnL = dead ? -__builtin_inff() : -mn * C2 + (float)PSH;
;     for (int r = 0; r < 16; ++r) p0[r] = fmaf(p0[r], C2, mnL); for (int r = 0; r < 16; ++r) p1[r] = fmaf(p1[r], C2, mnL);
.LBB0_1255:
	v_max_f32_e32 v2, v162, v163
	v_max_f32_e32 v4, v164, v165
	v_max_f32_e32 v5, v148, v149
	v_max3_f32 v6, v146, v147, v150
	v_max3_f32 v5, v5, v152, v153
	v_max3_f32 v2, v2, v166, v167
	v_max3_f32 v4, v4, v168, v169
	v_max3_f32 v6, v6, v151, v154
	v_max3_f32 v5, v5, v156, v157
	v_max3_f32 v2, v2, v170, v171
	v_max3_f32 v4, v4, v172, v173
	v_max3_f32 v6, v6, v155, v158
	v_max3_f32 v5, v5, v160, v161
	v_max3_f32 v2, v2, v174, v175
	v_max3_f32 v4, v4, v176, v177
	v_max3_f32 v5, v6, v159, v5
	v_max3_f32 v2, v2, v4, v5
	v_mov_b32_e32 v4, v2
	s_nop 1
	v_permlane32_swap_b32_e32 v2, v4
	v_max_f32_e32 v2, v2, v4
	v_max_f32_e32 v5, v219, v219
	v_max_f32_e32 v16, v5, v2
	v_sub_f32_e32 v4, v2, v219
	v_sub_f32_e32 v2, v219, v16
	v_mul_f32_e32 v2, 0x3a0293ee, v2
	v_mul_f32_e32 v4, 0x39b504f3, v4
	v_exp_f32_e32 v2, v2
	v_cmp_ge_f32_e32 vcc, 2.0, v4
	s_cmp_eq_u64 vcc, exec
	s_cselect_b64 s[6:7], -1, 0
	v_cndmask_b32_e64 v2, v2, 1.0, s[6:7]
	v_cmp_gt_f32_e32 vcc, 1.0, v2
	s_cbranch_vccz .LBB0_1259
	s_and_saveexec_b64 s[8:9], s[4:5]
	ds_write_b32 v222, v2 offset:128
	s_or_b64 exec, exec, s[8:9]
	s_waitcnt lgkmcnt(0)
	v_add_u32_e32 v4, s93, v223
	ds_read_b128 v[194:197], v4 offset:224
	ds_read_b128 v[12:15], v4 offset:192
	ds_read_b128 v[8:11], v4 offset:160
	ds_read_b128 v[4:7], v4 offset:128
	s_waitcnt lgkmcnt(0)
	v_pk_mul_f32 v[142:143], v[142:143], v[194:195]
	v_pk_mul_f32 v[138:139], v[138:139], v[12:13]
	v_pk_mul_f32 v[134:135], v[134:135], v[8:9]
	v_pk_mul_f32 v[144:145], v[144:145], v[196:197]
	v_pk_mul_f32 v[140:141], v[140:141], v[14:15]
	v_pk_mul_f32 v[136:137], v[136:137], v[10:11]
	v_pk_mul_f32 v[132:133], v[132:133], v[6:7]
	v_pk_mul_f32 v[130:131], v[130:131], v[4:5]
	v_pk_mul_f32 v[126:127], v[126:127], v[194:195]
	v_pk_mul_f32 v[122:123], v[122:123], v[12:13]
	v_pk_mul_f32 v[118:119], v[118:119], v[8:9]
	v_pk_mul_f32 v[128:129], v[128:129], v[196:197]
	v_pk_mul_f32 v[124:125], v[124:125], v[14:15]
	v_pk_mul_f32 v[120:121], v[120:121], v[10:11]
	v_pk_mul_f32 v[116:117], v[116:117], v[6:7]
	v_pk_mul_f32 v[114:115], v[114:115], v[4:5]
	v_pk_mul_f32 v[110:111], v[110:111], v[194:195]
	v_pk_mul_f32 v[106:107], v[106:107], v[12:13]
	v_pk_mul_f32 v[102:103], v[102:103], v[8:9]
	v_pk_mul_f32 v[112:113], v[112:113], v[196:197]
	v_pk_mul_f32 v[108:109], v[108:109], v[14:15]
	v_pk_mul_f32 v[104:105], v[104:105], v[10:11]
	v_pk_mul_f32 v[100:101], v[100:101], v[6:7]
	v_pk_mul_f32 v[98:99], v[98:99], v[4:5]
	v_pk_mul_f32 v[94:95], v[94:95], v[194:195]
	v_pk_mul_f32 v[90:91], v[90:91], v[12:13]
	v_pk_mul_f32 v[86:87], v[86:87], v[8:9]
	v_pk_mul_f32 v[96:97], v[96:97], v[196:197]
	v_pk_mul_f32 v[92:93], v[92:93], v[14:15]
	v_pk_mul_f32 v[88:89], v[88:89], v[10:11]
	v_pk_mul_f32 v[84:85], v[84:85], v[6:7]
	v_pk_mul_f32 v[82:83], v[82:83], v[4:5]
	v_pk_mul_f32 v[78:79], v[78:79], v[194:195]
	v_pk_mul_f32 v[74:75], v[74:75], v[12:13]
	v_pk_mul_f32 v[70:71], v[70:71], v[8:9]
	v_pk_mul_f32 v[80:81], v[80:81], v[196:197]
	v_pk_mul_f32 v[76:77], v[76:77], v[14:15]
	v_pk_mul_f32 v[72:73], v[72:73], v[10:11]
	v_pk_mul_f32 v[68:69], v[68:69], v[6:7]
	v_pk_mul_f32 v[66:67], v[66:67], v[4:5]
	v_pk_mul_f32 v[62:63], v[62:63], v[194:195]
	v_pk_mul_f32 v[58:59], v[58:59], v[12:13]
	v_pk_mul_f32 v[54:55], v[54:55], v[8:9]
	v_pk_mul_f32 v[64:65], v[64:65], v[196:197]
	v_pk_mul_f32 v[60:61], v[60:61], v[14:15]
	v_pk_mul_f32 v[56:57], v[56:57], v[10:11]
	v_pk_mul_f32 v[52:53], v[52:53], v[6:7]
	v_pk_mul_f32 v[50:51], v[50:51], v[4:5]
	v_pk_mul_f32 v[46:47], v[46:47], v[194:195]
	v_pk_mul_f32 v[42:43], v[42:43], v[12:13]
	v_pk_mul_f32 v[38:39], v[38:39], v[8:9]
	v_pk_mul_f32 v[48:49], v[48:49], v[196:197]
	v_pk_mul_f32 v[44:45], v[44:45], v[14:15]
	v_pk_mul_f32 v[40:41], v[40:41], v[10:11]
	v_pk_mul_f32 v[36:37], v[36:37], v[6:7]
	v_pk_mul_f32 v[34:35], v[34:35], v[4:5]
	v_pk_mul_f32 v[30:31], v[30:31], v[194:195]
	v_pk_mul_f32 v[26:27], v[26:27], v[12:13]
	v_pk_mul_f32 v[22:23], v[22:23], v[8:9]
	v_pk_mul_f32 v[32:33], v[32:33], v[196:197]
	v_pk_mul_f32 v[28:29], v[28:29], v[14:15]
	v_pk_mul_f32 v[24:25], v[24:25], v[10:11]
	v_pk_mul_f32 v[20:21], v[20:21], v[6:7]
	v_pk_mul_f32 v[18:19], v[18:19], v[4:5]

; __device__ __forceinline__ void finishSM8(f32x16& p0, f32x16& p1, float alpha, float& l_reg, i32x8& pa) {
;     for (int r = 0; r < 16; ++r) p1[r] = __builtin_amdgcn_exp2f(p1[r]);
;     float ps;
;     { float s0 = p0[0] + p0[1], s1 = p0[2] + p0[3], s2 = p1[0] + p1[1], s3 = p1[2] + p1[3];
; #pragma unroll
;       for (int r = 4; r < 16; r += 4) { s0 += p0[r]; s0 += p0[r + 1]; s1 += p0[r + 2]; s1 += p0[r + 3]; s2 += p1[r]; s2 += p1[r + 1]; s3 += p1[r + 2]; s3 += p1[r + 3]; }
;       ps = (s0 + s1) + (s2 + s3); }
;     { auto rr = __builtin_amdgcn_permlane32_swap(__float_as_uint(ps), __float_as_uint(ps), false, false);
;       ps = __uint_as_float(rr[0]) + __uint_as_float(rr[1]); }
;     l_reg = l_reg * alpha + ps;
; #pragma unroll
;     for (int d = 0; d < 4; ++d) { int w0 = 0, w1 = 0;
;         w0 = __builtin_amdgcn_cvt_pk_fp8_f32(p0[4 * d], p0[4 * d + 1], w0, false); w0 = __builtin_amdgcn_cvt_pk_fp8_f32(p0[4 * d + 2], p0[4 * d + 3], w0, true);
;         w1 = __builtin_amdgcn_cvt_pk_fp8_f32(p1[4 * d], p1[4 * d + 1], w1, false); w1 = __builtin_amdgcn_cvt_pk_fp8_f32(p1[4 * d + 2], p1[4 * d + 3], w1, true);
;         pa[d] = w0; pa[4 + d] = w1; }
.LBB0_1265:
	ds_read_b128 v[232:235], v203
	ds_read_b128 v[236:239], v214
	ds_read_b128 v[240:243], v203 offset:2048
	ds_read_b128 v[244:247], v214 offset:2048
	v_add_f32_e32 v254, v154, v155
	v_add_f32_e32 v255, v10, v12
	v_add_f32_e32 v166, v164, v165
	v_add_f32_e32 v167, v158, v159
	v_add_f32_e32 v254, v150, v254
	v_add_f32_e32 v255, v14, v255
	v_add_f32_e32 v166, v162, v166
	v_add_f32_e32 v167, v160, v167
	v_add_f32_e32 v254, v151, v254
	v_add_f32_e32 v255, v15, v255
	v_add_f32_e32 v166, v163, v166
	v_add_f32_e32 v167, v161, v167
	v_add_f32_e32 v254, v11, v254
	v_add_f32_e32 v255, v4, v255
	v_add_f32_e32 v166, v156, v166
	v_add_f32_e32 v167, v146, v167
	v_add_f32_e32 v254, v13, v254
	v_add_f32_e32 v255, v5, v255
	v_add_f32_e32 v166, v157, v166
	v_add_f32_e32 v167, v147, v167
	v_add_f32_e32 v254, v8, v254
	v_add_f32_e32 v255, v6, v255
	v_add_f32_e32 v166, v152, v166
	v_add_f32_e32 v167, v148, v167
	v_add_f32_e32 v254, v9, v254
	v_add_f32_e32 v255, v7, v255
	v_add_f32_e32 v166, v153, v166
	v_add_f32_e32 v167, v149, v167
	v_add_f32_e32 v254, v255, v254
	v_add_f32_e32 v255, v166, v167
	v_add_f32_e32 v217, v255, v254
	v_mov_b32_e32 v218, v217
	s_nop 1
	v_permlane32_swap_b32_e32 v217, v218
	v_cvt_pk_fp8_f32 v166, v154, v155
	v_cvt_pk_fp8_f32 v170, v164, v165
	v_cvt_pk_fp8_f32 v167, v150, v151
	v_cvt_pk_fp8_f32 v171, v162, v163
	v_cvt_pk_fp8_f32 v168, v11, v13
	v_cvt_pk_fp8_f32 v172, v156, v157
	v_cvt_pk_fp8_f32 v169, v8, v9
	v_cvt_pk_fp8_f32 v173, v152, v153
	v_cvt_pk_fp8_f32 v166, v10, v12 op_sel:[0,0,1]
	v_cvt_pk_fp8_f32 v170, v158, v159 op_sel:[0,0,1]
	v_cvt_pk_fp8_f32 v167, v14, v15 op_sel:[0,0,1]
	v_cvt_pk_fp8_f32 v171, v160, v161 op_sel:[0,0,1]
	v_cvt_pk_fp8_f32 v168, v4, v5 op_sel:[0,0,1]
	v_cvt_pk_fp8_f32 v172, v146, v147 op_sel:[0,0,1]
	v_cvt_pk_fp8_f32 v169, v6, v7 op_sel:[0,0,1]
	v_cvt_pk_fp8_f32 v173, v148, v149 op_sel:[0,0,1]
	ds_read_b128 v[4:7], v203 offset:4096
	ds_read_b128 v[8:11], v214 offset:4096
	ds_read_b128 v[146:149], v203 offset:6144
	ds_read_b128 v[150:153], v214 offset:6144
	s_waitcnt lgkmcnt(4)
	v_mfma_f32_32x32x64_f8f6f4 v[130:145], v[166:173], v[232:239], v[130:145]
	ds_read_b128 v[232:235], v203 offset:16384
	ds_read_b128 v[236:239], v214 offset:16384
	v_mfma_f32_32x32x64_f8f6f4 v[114:129], v[166:173], v[240:247], v[114:129]
	ds_read_b128 v[240:243], v203 offset:18432
	ds_read_b128 v[244:247], v214 offset:18432
	s_waitcnt lgkmcnt(4)
	v_mfma_f32_32x32x64_f8f6f4 v[98:113], v[166:173], v[4:11], v[98:113]
	ds_read_b128 v[4:7], v203 offset:20480
	ds_read_b128 v[8:11], v214 offset:20480
	v_mfma_f32_32x32x64_f8f6f4 v[82:97], v[166:173], v[146:153], v[82:97]
	ds_read_b128 v[146:149], v203 offset:22528
	ds_read_b128 v[150:153], v214 offset:22528
	s_waitcnt lgkmcnt(4)
	v_mfma_f32_32x32x64_f8f6f4 v[66:81], v[166:173], v[232:239], v[66:81]
	v_mfma_f32_32x32x64_f8f6f4 v[50:65], v[166:173], v[240:247], v[50:65]
	s_waitcnt lgkmcnt(0)
	v_mfma_f32_32x32x64_f8f6f4 v[34:49], v[166:173], v[4:11], v[34:49]
	v_mfma_f32_32x32x64_f8f6f4 v[18:33], v[166:173], v[146:153], v[18:33]
	s_nop 15
	s_nop 15
	s_mov_b64 s[6:7], -1
	s_and_b64 vcc, exec, s[70:71]
	s_cbranch_vccz .LBB0_1267
	s_waitcnt vmcnt(0) lgkmcnt(0)
	s_mov_b64 s[6:7], 0

;     float pmax;
;     { float m0 = fmaxf(p0[0], p0[1]), m1 = fmaxf(p0[2], p0[3]), m2 = fmaxf(p1[0], p1[1]), m3 = fmaxf(p1[2], p1[3]);
; #pragma unroll
;       for (int r = 4; r < 16; r += 4) { m0 = fmaxf(fmaxf(m0, p0[r]), p0[r + 1]); m1 = fmaxf(fmaxf(m1, p0[r + 2]), p0[r + 3]); m2 = fmaxf(fmaxf(m2, p1[r]), p1[r + 1]); m3 = fmaxf(fmaxf(m3, p1[r + 2]), p1[r + 3]); }
;       pmax = fmaxf(fmaxf(m0, m1), fmaxf(m2, m3)); }
;     pmax = dead ? -__builtin_inff() : pmax;
;     { auto rr = __builtin_amdgcn_permlane32_swap(__float_as_uint(pmax), __float_as_uint(pmax), false, false);
;       pmax = fmaxf(__uint_as_float(rr[0]), __uint_as_float(rr[1])); }
;     constexpr float SCL = SCALE / (float)(1 << SH), C2 = 1.4426950408889634f * SCL;
;     if (__builtin_expect(__all((pmax - m_reg) * SCL <= (float)THRI), 1)) { mn = m_reg; alpha = 1.f; }
;     else { mn = fmaxf(m_reg, pmax); alpha = __builtin_amdgcn_exp2f((m_reg - mn) * C2); m_reg = mn; }
;     const float mnL = dead ? -__builtin_inff() : -mn * C2 + (float)PSH;
;     for (int r = 0; r < 16; ++r) p0[r] = fmaf(p0[r], C2, mnL); for (int r = 0; r < 16; ++r) p1[r] = fmaf(p1[r], C2, mnL);
.LBB0_1273:
	v_max_f32_e32 v4, v162, v163
	v_max_f32_e32 v5, v164, v165
	v_max_f32_e32 v6, v148, v149
	v_max3_f32 v7, v146, v147, v150
	v_max3_f32 v6, v6, v152, v153
	v_max3_f32 v4, v4, v166, v167
	v_max3_f32 v5, v5, v168, v169
	v_max3_f32 v7, v7, v151, v154
	v_max3_f32 v6, v6, v156, v157
	v_max3_f32 v4, v4, v170, v171
	v_max3_f32 v5, v5, v172, v173
	v_max3_f32 v7, v7, v155, v158
	v_max3_f32 v6, v6, v160, v161
	v_max3_f32 v4, v4, v174, v175
	v_max3_f32 v5, v5, v176, v177
	v_max3_f32 v6, v7, v159, v6
	v_max3_f32 v4, v4, v5, v6
	v_mov_b32_e32 v5, v4
	s_nop 1
	v_permlane32_swap_b32_e32 v4, v5
	v_max_f32_e32 v4, v4, v5
	v_max_f32_e32 v6, v219, v219
	v_max_f32_e32 v209, v6, v4
	v_sub_f32_e32 v5, v4, v219
	v_sub_f32_e32 v4, v219, v209
	v_mul_f32_e32 v4, 0x3a0293ee, v4
	v_mul_f32_e32 v5, 0x39b504f3, v5
	v_exp_f32_e32 v4, v4
	v_cmp_ge_f32_e32 vcc, 2.0, v5
	s_cmp_eq_u64 vcc, exec
	s_cselect_b64 s[6:7], -1, 0
	v_readlane_b32 s66, v253, 52
	v_cndmask_b32_e64 v208, v4, 1.0, s[6:7]
	v_readlane_b32 s67, v253, 53
	v_cmp_gt_f32_e32 vcc, 1.0, v208
	s_cbranch_vccz .LBB0_1277
	s_and_saveexec_b64 s[8:9], s[4:5]
	ds_write_b32 v222, v208 offset:128
	s_or_b64 exec, exec, s[8:9]
	s_waitcnt lgkmcnt(0)
	v_add_u32_e32 v4, s93, v223
	ds_read_b128 v[194:197], v4 offset:224
	ds_read_b128 v[12:15], v4 offset:192
	ds_read_b128 v[8:11], v4 offset:160
	ds_read_b128 v[4:7], v4 offset:128
	s_waitcnt lgkmcnt(0)
	v_pk_mul_f32 v[142:143], v[142:143], v[194:195]
	v_pk_mul_f32 v[138:139], v[138:139], v[12:13]
	v_pk_mul_f32 v[134:135], v[134:135], v[8:9]
	v_pk_mul_f32 v[144:145], v[144:145], v[196:197]
	v_pk_mul_f32 v[140:141], v[140:141], v[14:15]
	v_pk_mul_f32 v[136:137], v[136:137], v[10:11]
	v_pk_mul_f32 v[132:133], v[132:133], v[6:7]
	v_pk_mul_f32 v[130:131], v[130:131], v[4:5]
	v_pk_mul_f32 v[126:127], v[126:127], v[194:195]
	v_pk_mul_f32 v[122:123], v[122:123], v[12:13]
	v_pk_mul_f32 v[118:119], v[118:119], v[8:9]
	v_pk_mul_f32 v[128:129], v[128:129], v[196:197]
	v_pk_mul_f32 v[124:125], v[124:125], v[14:15]
	v_pk_mul_f32 v[120:121], v[120:121], v[10:11]
	v_pk_mul_f32 v[116:117], v[116:117], v[6:7]
	v_pk_mul_f32 v[114:115], v[114:115], v[4:5]
	v_pk_mul_f32 v[110:111], v[110:111], v[194:195]
	v_pk_mul_f32 v[106:107], v[106:107], v[12:13]
	v_pk_mul_f32 v[102:103], v[102:103], v[8:9]
	v_pk_mul_f32 v[112:113], v[112:113], v[196:197]
	v_pk_mul_f32 v[108:109], v[108:109], v[14:15]
	v_pk_mul_f32 v[104:105], v[104:105], v[10:11]
	v_pk_mul_f32 v[100:101], v[100:101], v[6:7]
	v_pk_mul_f32 v[98:99], v[98:99], v[4:5]
	v_pk_mul_f32 v[94:95], v[94:95], v[194:195]
	v_pk_mul_f32 v[90:91], v[90:91], v[12:13]
	v_pk_mul_f32 v[86:87], v[86:87], v[8:9]
	v_pk_mul_f32 v[96:97], v[96:97], v[196:197]
	v_pk_mul_f32 v[92:93], v[92:93], v[14:15]
	v_pk_mul_f32 v[88:89], v[88:89], v[10:11]
	v_pk_mul_f32 v[84:85], v[84:85], v[6:7]
	v_pk_mul_f32 v[82:83], v[82:83], v[4:5]
	v_pk_mul_f32 v[78:79], v[78:79], v[194:195]
	v_pk_mul_f32 v[74:75], v[74:75], v[12:13]
	v_pk_mul_f32 v[70:71], v[70:71], v[8:9]
	v_pk_mul_f32 v[80:81], v[80:81], v[196:197]
	v_pk_mul_f32 v[76:77], v[76:77], v[14:15]
	v_pk_mul_f32 v[72:73], v[72:73], v[10:11]
	v_pk_mul_f32 v[68:69], v[68:69], v[6:7]
	v_pk_mul_f32 v[66:67], v[66:67], v[4:5]
	v_pk_mul_f32 v[62:63], v[62:63], v[194:195]
	v_pk_mul_f32 v[58:59], v[58:59], v[12:13]
	v_pk_mul_f32 v[54:55], v[54:55], v[8:9]
	v_pk_mul_f32 v[64:65], v[64:65], v[196:197]
	v_pk_mul_f32 v[60:61], v[60:61], v[14:15]
	v_pk_mul_f32 v[56:57], v[56:57], v[10:11]
	v_pk_mul_f32 v[52:53], v[52:53], v[6:7]
	v_pk_mul_f32 v[50:51], v[50:51], v[4:5]
	v_pk_mul_f32 v[46:47], v[46:47], v[194:195]
	v_pk_mul_f32 v[42:43], v[42:43], v[12:13]
	v_pk_mul_f32 v[38:39], v[38:39], v[8:9]
	v_pk_mul_f32 v[48:49], v[48:49], v[196:197]
	v_pk_mul_f32 v[44:45], v[44:45], v[14:15]
	v_pk_mul_f32 v[40:41], v[40:41], v[10:11]
	v_pk_mul_f32 v[36:37], v[36:37], v[6:7]
	v_pk_mul_f32 v[34:35], v[34:35], v[4:5]
	v_pk_mul_f32 v[30:31], v[30:31], v[194:195]
	v_pk_mul_f32 v[26:27], v[26:27], v[12:13]
	v_pk_mul_f32 v[22:23], v[22:23], v[8:9]
	v_pk_mul_f32 v[32:33], v[32:33], v[196:197]
	v_pk_mul_f32 v[28:29], v[28:29], v[14:15]
	v_pk_mul_f32 v[24:25], v[24:25], v[10:11]
	v_pk_mul_f32 v[20:21], v[20:21], v[6:7]
	v_pk_mul_f32 v[18:19], v[18:19], v[4:5]

; __device__ __forceinline__ void finishSM8(f32x16& p0, f32x16& p1, float alpha, float& l_reg, i32x8& pa) {
;     for (int r = 0; r < 16; ++r) p1[r] = __builtin_amdgcn_exp2f(p1[r]);
;     float ps;
;     { float s0 = p0[0] + p0[1], s1 = p0[2] + p0[3], s2 = p1[0] + p1[1], s3 = p1[2] + p1[3];
; #pragma unroll
;       for (int r = 4; r < 16; r += 4) { s0 += p0[r]; s0 += p0[r + 1]; s1 += p0[r + 2]; s1 += p0[r + 3]; s2 += p1[r]; s2 += p1[r + 1]; s3 += p1[r + 2]; s3 += p1[r + 3]; }
;       ps = (s0 + s1) + (s2 + s3); }
;     { auto rr = __builtin_amdgcn_permlane32_swap(__float_as_uint(ps), __float_as_uint(ps), false, false);
;       ps = __uint_as_float(rr[0]) + __uint_as_float(rr[1]); }
;     l_reg = l_reg * alpha + ps;
; #pragma unroll
;     for (int d = 0; d < 4; ++d) { int w0 = 0, w1 = 0;
;         w0 = __builtin_amdgcn_cvt_pk_fp8_f32(p0[4 * d], p0[4 * d + 1], w0, false); w0 = __builtin_amdgcn_cvt_pk_fp8_f32(p0[4 * d + 2], p0[4 * d + 3], w0, true);
;         w1 = __builtin_amdgcn_cvt_pk_fp8_f32(p1[4 * d], p1[4 * d + 1], w1, false); w1 = __builtin_amdgcn_cvt_pk_fp8_f32(p1[4 * d + 2], p1[4 * d + 3], w1, true);
;         pa[d] = w0; pa[4 + d] = w1; }
.LBB0_1283:
	ds_read_b128 v[232:235], v203 offset:32768
	ds_read_b128 v[236:239], v214 offset:32768
	ds_read_b128 v[240:243], v203 offset:34816
	ds_read_b128 v[244:247], v214 offset:34816
	v_add_f32_e32 v4, v156, v157
	v_add_f32_e32 v5, v12, v14
	v_add_f32_e32 v168, v166, v167
	v_add_f32_e32 v169, v160, v161
	v_add_f32_e32 v4, v152, v4
	v_add_f32_e32 v5, v146, v5
	v_add_f32_e32 v168, v164, v168
	v_add_f32_e32 v169, v162, v169
	v_add_f32_e32 v4, v153, v4
	v_add_f32_e32 v5, v147, v5
	v_add_f32_e32 v168, v165, v168
	v_add_f32_e32 v169, v163, v169
	v_add_f32_e32 v4, v13, v4
	v_add_f32_e32 v5, v6, v5
	v_add_f32_e32 v168, v158, v168
	v_add_f32_e32 v169, v148, v169
	v_add_f32_e32 v4, v15, v4
	v_add_f32_e32 v5, v7, v5
	v_add_f32_e32 v168, v159, v168
	v_add_f32_e32 v169, v149, v169
	v_add_f32_e32 v4, v10, v4
	v_add_f32_e32 v5, v8, v5
	v_add_f32_e32 v168, v154, v168
	v_add_f32_e32 v169, v150, v169
	v_add_f32_e32 v4, v11, v4
	v_add_f32_e32 v5, v9, v5
	v_add_f32_e32 v168, v155, v168
	v_add_f32_e32 v169, v151, v169
	v_add_f32_e32 v4, v5, v4
	v_add_f32_e32 v5, v168, v169
	v_add_f32_e32 v4, v5, v4
	v_mov_b32_e32 v5, v4
	s_nop 1
	v_permlane32_swap_b32_e32 v4, v5
	v_cvt_pk_fp8_f32 v168, v156, v157
	v_cvt_pk_fp8_f32 v172, v166, v167
	v_cvt_pk_fp8_f32 v169, v152, v153
	v_cvt_pk_fp8_f32 v173, v164, v165
	v_cvt_pk_fp8_f32 v170, v13, v15
	v_cvt_pk_fp8_f32 v174, v158, v159
	v_cvt_pk_fp8_f32 v171, v10, v11
	v_cvt_pk_fp8_f32 v175, v154, v155
	v_cvt_pk_fp8_f32 v168, v12, v14 op_sel:[0,0,1]
	v_cvt_pk_fp8_f32 v172, v160, v161 op_sel:[0,0,1]
	v_cvt_pk_fp8_f32 v169, v146, v147 op_sel:[0,0,1]
	v_cvt_pk_fp8_f32 v173, v162, v163 op_sel:[0,0,1]
	v_cvt_pk_fp8_f32 v170, v6, v7 op_sel:[0,0,1]
	v_cvt_pk_fp8_f32 v174, v148, v149 op_sel:[0,0,1]
	v_cvt_pk_fp8_f32 v171, v8, v9 op_sel:[0,0,1]
	v_cvt_pk_fp8_f32 v175, v150, v151 op_sel:[0,0,1]
	ds_read_b128 v[6:9], v203 offset:36864
	ds_read_b128 v[10:13], v214 offset:36864
	ds_read_b128 v[146:149], v203 offset:38912
	ds_read_b128 v[150:153], v214 offset:38912
	s_waitcnt lgkmcnt(4)
	v_mfma_f32_32x32x64_f8f6f4 v[130:145], v[168:175], v[232:239], v[130:145]
	ds_read_b128 v[232:235], v203 offset:49152
	ds_read_b128 v[236:239], v214 offset:49152
	v_mfma_f32_32x32x64_f8f6f4 v[114:129], v[168:175], v[240:247], v[114:129]
	ds_read_b128 v[240:243], v203 offset:51200
	ds_read_b128 v[244:247], v214 offset:51200
	s_waitcnt lgkmcnt(4)
	v_mfma_f32_32x32x64_f8f6f4 v[98:113], v[168:175], v[6:13], v[98:113]
	ds_read_b128 v[6:9], v203 offset:53248
	ds_read_b128 v[10:13], v214 offset:53248
	v_mfma_f32_32x32x64_f8f6f4 v[82:97], v[168:175], v[146:153], v[82:97]
	ds_read_b128 v[146:149], v203 offset:55296
	ds_read_b128 v[150:153], v214 offset:55296
	s_waitcnt lgkmcnt(4)
	v_mfma_f32_32x32x64_f8f6f4 v[66:81], v[168:175], v[232:239], v[66:81]
	v_mfma_f32_32x32x64_f8f6f4 v[50:65], v[168:175], v[240:247], v[50:65]
	s_waitcnt lgkmcnt(0)
	v_mfma_f32_32x32x64_f8f6f4 v[34:49], v[168:175], v[6:13], v[34:49]
	v_mfma_f32_32x32x64_f8f6f4 v[18:33], v[168:175], v[146:153], v[18:33]
	s_nop 15
	s_nop 15
	s_mov_b64 s[6:7], -1
	s_and_b64 vcc, exec, s[70:71]
	s_cbranch_vccz .LBB0_1285
	s_waitcnt vmcnt(0) lgkmcnt(0)
	s_mov_b64 s[6:7], 0

; #define GAS __attribute__((address_space(1)))
; __global__ void __launch_bounds__(NWAVES * 64, 2) mk_fwd(Args args) {
;     ...
;     if (IN(10)) {
;         const GAS f32x4* gr = (const GAS f32x4*)final_g + 2 * lane;
;         for (int m = gw; m < MTOK; m += NGW) {
;             const GAS v4u* xr = (const GAS v4u*)(XB + (size_t)m * DMODEL) + lane;
;             GAS f32x4* orow = (GAS f32x4*)(out + (size_t)m * DMODEL) + 2 * lane;
;             const float rs = rsqrtf(__hip_atomic_load(SS3 + m, __ATOMIC_RELAXED, __HIP_MEMORY_SCOPE_AGENT) * (1.0f / DMODEL) + 1e-5f);
; #pragma unroll
;             for (int j = 0; j < 8; ++j) { const v4u w = __builtin_nontemporal_load(xr + 64 * j); const f32x4 g0 = gr[128 * j], g1 = gr[128 * j + 1];
;                 const f32x4 a0 = {__uint_as_float(w.x << 16), __uint_as_float(w.x & 0xffff0000u), __uint_as_float(w.y << 16), __uint_as_float(w.y & 0xffff0000u)};
;                 const f32x4 a1 = {__uint_as_float(w.z << 16), __uint_as_float(w.z & 0xffff0000u), __uint_as_float(w.w << 16), __uint_as_float(w.w & 0xffff0000u)};
;                 __builtin_nontemporal_store(a0 * rs * g0, orow + 128 * j); __builtin_nontemporal_store(a1 * rs * g1, orow + 128 * j + 1); }
;         }
.LBB0_2431:
	s_cmp_lt_i32 s80, 11
	s_cselect_b64 s[0:1], -1, 0
	s_cmp_gt_i32 s81, 10
	s_cselect_b64 s[2:3], -1, 0
	s_and_b64 s[0:1], s[0:1], s[2:3]
	s_andn2_b64 vcc, exec, s[0:1]
	s_cbranch_vccnz .LBB0_2435
	s_cmpk_gt_i32 s90, 0x3fff
	s_cbranch_scc1 .LBB0_2435
	v_readlane_b32 s0, v253, 0
	v_lshlrev_b32_e32 v0, 5, v216
	v_mov_b32_e32 v1, 0
	v_readlane_b32 s1, v253, 1
	v_readlane_b32 s6, v253, 6
	v_readlane_b32 s7, v253, 7
	s_mov_b64 s[0:1], 0x1000
	s_ashr_i32 s91, s90, 31
	s_waitcnt lgkmcnt(0)
	v_lshl_add_u64 v[2:3], s[6:7], 0, v[0:1]
	v_lshl_add_u64 v[4:5], v[2:3], 0, s[0:1]
	s_mov_b64 s[0:1], 0x1800
	v_lshl_add_u64 v[6:7], v[2:3], 0, s[0:1]
	s_mov_b64 s[0:1], 0x2000
	v_lshl_add_u64 v[8:9], v[2:3], 0, s[0:1]
	s_mov_b64 s[0:1], 0x2800
	v_lshl_add_u64 v[10:11], v[2:3], 0, s[0:1]
	s_mov_b64 s[0:1], 0x3000
	v_lshl_add_u64 v[12:13], v[2:3], 0, s[0:1]
	s_mov_b64 s[0:1], 0x3800
	v_lshl_add_u64 v[14:15], v[2:3], 0, s[0:1]
	s_lshl_b64 s[0:1], s[90:91], 2
	v_readlane_b32 s2, v253, 2
	v_readlane_b32 s3, v253, 3
	s_add_u32 s8, s0, 0x28000
	v_readlane_b32 s4, v253, 4
	v_readlane_b32 s5, v253, 5
	s_addc_u32 s9, s1, 0
	s_ashr_i32 s85, s84, 31
	s_lshl_b64 s[2:3], s[90:91], 13
	s_lshl_b64 s[0:1], s[84:85], 2
	v_lshl_or_b32 v16, v216, 4, s2
	v_mov_b32_e32 v17, s3
	s_lshl_b64 s[2:3], s[84:85], 13
	s_lshl_b64 s[4:5], s[90:91], 14
	s_add_u32 s4, s76, s4
	s_addc_u32 s5, s77, s5
	v_lshl_add_u64 v[18:19], s[4:5], 0, v[0:1]
	s_mov_b64 s[4:5], 0x3810
	v_lshl_add_u64 v[18:19], v[18:19], 0, s[4:5]
	s_lshl_b64 s[4:5], s[84:85], 14
	v_mov_b32_e32 v22, 0x3727c5ac
	s_mov_b32 s10, 0x800000
	s_mov_b32 s11, 0x10400000
	s_movk_i32 s12, 0xd000
	s_movk_i32 s13, 0xe000
	s_mov_b32 s14, 0x10401000
	s_movk_i32 s15, 0xf000
	s_mov_b32 s98, 0x10400000
	s_mov_b32 s99, 0
	s_mov_b32 s100, 0x1000
	s_mov_b32 s101, 0
	s_mov_b32 s12, 0xffffd7f0
	s_mov_b32 s13, -1
	s_mov_b32 s14, 0xfffff7f0
	s_mov_b32 s15, -1
	global_load_dwordx4 v[48:51], v[2:3], off
	global_load_dwordx4 v[52:55], v[2:3], off offset:16
	global_load_dwordx4 v[56:59], v[2:3], off offset:2048
	global_load_dwordx4 v[60:63], v[2:3], off offset:2064
	global_load_dwordx4 v[64:67], v[4:5], off
	global_load_dwordx4 v[68:71], v[4:5], off offset:16
	global_load_dwordx4 v[72:75], v[6:7], off
	global_load_dwordx4 v[76:79], v[6:7], off offset:16
	global_load_dwordx4 v[80:83], v[8:9], off
	global_load_dwordx4 v[84:87], v[8:9], off offset:16
	global_load_dwordx4 v[88:91], v[10:11], off
	global_load_dwordx4 v[92:95], v[10:11], off offset:16
	global_load_dwordx4 v[96:99], v[12:13], off
	global_load_dwordx4 v[100:103], v[12:13], off offset:16
	global_load_dwordx4 v[104:107], v[14:15], off
	global_load_dwordx4 v[108:111], v[14:15], off offset:16
.LBB0_2434:
	s_add_u32 s6, s78, s8
	s_addc_u32 s7, s79, s9
	global_load_dword v0, v1, s[6:7] sc1
	v_lshl_add_u64 v[20:21], s[78:79], 0, v[16:17]
	v_lshl_add_u64 v[20:21], v[20:21], 0, s[98:99]
	v_lshl_add_u64 v[40:41], v[20:21], 0, s[100:101]
	global_load_dwordx4 v[112:115], v[20:21], off nt
	global_load_dwordx4 v[116:119], v[20:21], off offset:1024 nt
	global_load_dwordx4 v[120:123], v[20:21], off offset:2048 nt
	global_load_dwordx4 v[124:127], v[20:21], off offset:3072 nt
	global_load_dwordx4 v[128:131], v[40:41], off nt
	global_load_dwordx4 v[132:135], v[40:41], off offset:1024 nt
	global_load_dwordx4 v[136:139], v[40:41], off offset:2048 nt
	global_load_dwordx4 v[140:143], v[40:41], off offset:3072 nt
	v_lshl_add_u64 v[36:37], v[18:19], 0, s[12:13]
	v_lshl_add_u64 v[38:39], v[18:19], 0, s[14:15]
	s_add_u32 s8, s8, s0
	s_addc_u32 s9, s9, s1
	v_lshl_add_u64 v[16:17], v[16:17], 0, s[2:3]
	v_lshl_add_u64 v[18:19], v[18:19], 0, s[4:5]
	s_add_i32 s90, s90, s84
	s_waitcnt vmcnt(8)
	v_fmamk_f32 v0, v0, 0x39800000, v22
	v_mul_f32_e32 v23, 0x4b800000, v0
	v_cmp_gt_f32_e32 vcc, s10, v0
	s_nop 1
	v_cndmask_b32_e32 v0, v0, v23, vcc
	v_rsq_f32_e32 v0, v0
	s_nop 1
	v_mul_f32_e32 v23, 0x45800000, v0
	v_cndmask_b32_e32 v0, v0, v23, vcc
	s_waitcnt vmcnt(7)
	v_lshlrev_b32_e32 v24, 16, v112
	v_and_b32_e32 v25, 0xffff0000, v112
	v_lshlrev_b32_e32 v26, 16, v113
	v_and_b32_e32 v27, 0xffff0000, v113
	v_lshlrev_b32_e32 v28, 16, v114
	v_and_b32_e32 v29, 0xffff0000, v114
	v_lshlrev_b32_e32 v30, 16, v115
	v_and_b32_e32 v31, 0xffff0000, v115
	v_pk_mul_f32 v[24:25], v[0:1], v[24:25] op_sel_hi:[0,1]
	v_pk_mul_f32 v[26:27], v[0:1], v[26:27] op_sel_hi:[0,1]
	v_pk_mul_f32 v[28:29], v[0:1], v[28:29] op_sel_hi:[0,1]
	v_pk_mul_f32 v[30:31], v[0:1], v[30:31] op_sel_hi:[0,1]
	v_pk_mul_f32 v[24:25], v[48:49], v[24:25]
	v_pk_mul_f32 v[26:27], v[50:51], v[26:27]
	v_pk_mul_f32 v[28:29], v[52:53], v[28:29]
	v_pk_mul_f32 v[30:31], v[54:55], v[30:31]
	global_store_dwordx4 v[36:37], v[24:27], off offset:-4096 nt
	global_store_dwordx4 v[36:37], v[28:31], off offset:-4080 nt
	s_waitcnt vmcnt(8)
	v_lshlrev_b32_e32 v144, 16, v116
	v_and_b32_e32 v145, 0xffff0000, v116
	v_lshlrev_b32_e32 v146, 16, v117
	v_and_b32_e32 v147, 0xffff0000, v117
	v_lshlrev_b32_e32 v148, 16, v118
	v_and_b32_e32 v149, 0xffff0000, v118
	v_lshlrev_b32_e32 v150, 16, v119
	v_and_b32_e32 v151, 0xffff0000, v119
	v_pk_mul_f32 v[144:145], v[0:1], v[144:145] op_sel_hi:[0,1]
	v_pk_mul_f32 v[146:147], v[0:1], v[146:147] op_sel_hi:[0,1]
	v_pk_mul_f32 v[148:149], v[0:1], v[148:149] op_sel_hi:[0,1]
	v_pk_mul_f32 v[150:151], v[0:1], v[150:151] op_sel_hi:[0,1]
	v_pk_mul_f32 v[144:145], v[56:57], v[144:145]
	v_pk_mul_f32 v[146:147], v[58:59], v[146:147]
	v_pk_mul_f32 v[148:149], v[60:61], v[148:149]
	v_pk_mul_f32 v[150:151], v[62:63], v[150:151]
	global_store_dwordx4 v[36:37], v[144:147], off offset:-2048 nt
	global_store_dwordx4 v[36:37], v[148:151], off offset:-2032 nt
	s_waitcnt vmcnt(9)
; #define GAS __attribute__((address_space(1)))
; __global__ void __launch_bounds__(NWAVES * 64, 2) mk_fwd(Args args) {
;     ...
;             const GAS v4u* xr = (const GAS v4u*)(XB + (size_t)m * DMODEL) + lane;
;             GAS f32x4* orow = (GAS f32x4*)(out + (size_t)m * DMODEL) + 2 * lane;
;             const float rs = rsqrtf(__hip_atomic_load(SS3 + m, __ATOMIC_RELAXED, __HIP_MEMORY_SCOPE_AGENT) * (1.0f / DMODEL) + 1e-5f);
; #pragma unroll
;             for (int j = 0; j < 8; ++j) { const v4u w = __builtin_nontemporal_load(xr + 64 * j); const f32x4 g0 = gr[128 * j], g1 = gr[128 * j + 1];
;                 const f32x4 a0 = {__uint_as_float(w.x << 16), __uint_as_float(w.x & 0xffff0000u), __uint_as_float(w.y << 16), __uint_as_float(w.y & 0xffff0000u)};
;                 const f32x4 a1 = {__uint_as_float(w.z << 16), __uint_as_float(w.z & 0xffff0000u), __uint_as_float(w.w << 16), __uint_as_float(w.w & 0xffff0000u)};
;                 __builtin_nontemporal_store(a0 * rs * g0, orow + 128 * j); __builtin_nontemporal_store(a1 * rs * g1, orow + 128 * j + 1); }
;         }
	v_lshlrev_b32_e32 v24, 16, v120
	v_and_b32_e32 v25, 0xffff0000, v120
	v_lshlrev_b32_e32 v26, 16, v121
	v_and_b32_e32 v27, 0xffff0000, v121
	v_lshlrev_b32_e32 v28, 16, v122
	v_and_b32_e32 v29, 0xffff0000, v122
	v_lshlrev_b32_e32 v30, 16, v123
	v_and_b32_e32 v31, 0xffff0000, v123
	v_pk_mul_f32 v[24:25], v[0:1], v[24:25] op_sel_hi:[0,1]
	v_pk_mul_f32 v[26:27], v[0:1], v[26:27] op_sel_hi:[0,1]
	v_pk_mul_f32 v[28:29], v[0:1], v[28:29] op_sel_hi:[0,1]
	v_pk_mul_f32 v[30:31], v[0:1], v[30:31] op_sel_hi:[0,1]
	v_pk_mul_f32 v[24:25], v[64:65], v[24:25]
	v_pk_mul_f32 v[26:27], v[66:67], v[26:27]
	v_pk_mul_f32 v[28:29], v[68:69], v[28:29]
	v_pk_mul_f32 v[30:31], v[70:71], v[30:31]
	global_store_dwordx4 v[36:37], v[24:27], off nt
	global_store_dwordx4 v[36:37], v[28:31], off offset:16 nt
	s_waitcnt vmcnt(10)
	v_lshlrev_b32_e32 v144, 16, v124
	v_and_b32_e32 v145, 0xffff0000, v124
	v_lshlrev_b32_e32 v146, 16, v125
	v_and_b32_e32 v147, 0xffff0000, v125
	v_lshlrev_b32_e32 v148, 16, v126
	v_and_b32_e32 v149, 0xffff0000, v126
	v_lshlrev_b32_e32 v150, 16, v127
	v_and_b32_e32 v151, 0xffff0000, v127
	v_pk_mul_f32 v[144:145], v[0:1], v[144:145] op_sel_hi:[0,1]
	v_pk_mul_f32 v[146:147], v[0:1], v[146:147] op_sel_hi:[0,1]
	v_pk_mul_f32 v[148:149], v[0:1], v[148:149] op_sel_hi:[0,1]
	v_pk_mul_f32 v[150:151], v[0:1], v[150:151] op_sel_hi:[0,1]
	v_pk_mul_f32 v[144:145], v[72:73], v[144:145]
	v_pk_mul_f32 v[146:147], v[74:75], v[146:147]
	v_pk_mul_f32 v[148:149], v[76:77], v[148:149]
	v_pk_mul_f32 v[150:151], v[78:79], v[150:151]
	global_store_dwordx4 v[36:37], v[144:147], off offset:2048 nt
	global_store_dwordx4 v[36:37], v[148:151], off offset:2064 nt
	s_waitcnt vmcnt(11)
	v_lshlrev_b32_e32 v24, 16, v128
	v_and_b32_e32 v25, 0xffff0000, v128
	v_lshlrev_b32_e32 v26, 16, v129
	v_and_b32_e32 v27, 0xffff0000, v129
	v_lshlrev_b32_e32 v28, 16, v130
	v_and_b32_e32 v29, 0xffff0000, v130
	v_lshlrev_b32_e32 v30, 16, v131
	v_and_b32_e32 v31, 0xffff0000, v131
	v_pk_mul_f32 v[24:25], v[0:1], v[24:25] op_sel_hi:[0,1]
	v_pk_mul_f32 v[26:27], v[0:1], v[26:27] op_sel_hi:[0,1]
	v_pk_mul_f32 v[28:29], v[0:1], v[28:29] op_sel_hi:[0,1]
	v_pk_mul_f32 v[30:31], v[0:1], v[30:31] op_sel_hi:[0,1]
	v_pk_mul_f32 v[24:25], v[80:81], v[24:25]
	v_pk_mul_f32 v[26:27], v[82:83], v[26:27]
	v_pk_mul_f32 v[28:29], v[84:85], v[28:29]
	v_pk_mul_f32 v[30:31], v[86:87], v[30:31]
	global_store_dwordx4 v[38:39], v[24:27], off offset:-4096 nt
	global_store_dwordx4 v[38:39], v[28:31], off offset:-4080 nt
	s_waitcnt vmcnt(12)
	v_lshlrev_b32_e32 v144, 16, v132
	v_and_b32_e32 v145, 0xffff0000, v132
	v_lshlrev_b32_e32 v146, 16, v133
	v_and_b32_e32 v147, 0xffff0000, v133
	v_lshlrev_b32_e32 v148, 16, v134
	v_and_b32_e32 v149, 0xffff0000, v134
	v_lshlrev_b32_e32 v150, 16, v135
	v_and_b32_e32 v151, 0xffff0000, v135
	v_pk_mul_f32 v[144:145], v[0:1], v[144:145] op_sel_hi:[0,1]
	v_pk_mul_f32 v[146:147], v[0:1], v[146:147] op_sel_hi:[0,1]
	v_pk_mul_f32 v[148:149], v[0:1], v[148:149] op_sel_hi:[0,1]
	v_pk_mul_f32 v[150:151], v[0:1], v[150:151] op_sel_hi:[0,1]
	v_pk_mul_f32 v[144:145], v[88:89], v[144:145]
	v_pk_mul_f32 v[146:147], v[90:91], v[146:147]
	v_pk_mul_f32 v[148:149], v[92:93], v[148:149]
	v_pk_mul_f32 v[150:151], v[94:95], v[150:151]
	global_store_dwordx4 v[38:39], v[144:147], off offset:-2048 nt
	global_store_dwordx4 v[38:39], v[148:151], off offset:-2032 nt
	s_waitcnt vmcnt(13)
	v_lshlrev_b32_e32 v24, 16, v136
	v_and_b32_e32 v25, 0xffff0000, v136
	v_lshlrev_b32_e32 v26, 16, v137
	v_and_b32_e32 v27, 0xffff0000, v137
	v_lshlrev_b32_e32 v28, 16, v138
	v_and_b32_e32 v29, 0xffff0000, v138
	v_lshlrev_b32_e32 v30, 16, v139
	v_and_b32_e32 v31, 0xffff0000, v139
	v_pk_mul_f32 v[24:25], v[0:1], v[24:25] op_sel_hi:[0,1]
	v_pk_mul_f32 v[26:27], v[0:1], v[26:27] op_sel_hi:[0,1]
	v_pk_mul_f32 v[28:29], v[0:1], v[28:29] op_sel_hi:[0,1]
	v_pk_mul_f32 v[30:31], v[0:1], v[30:31] op_sel_hi:[0,1]
	v_pk_mul_f32 v[24:25], v[96:97], v[24:25]
	v_pk_mul_f32 v[26:27], v[98:99], v[26:27]
	v_pk_mul_f32 v[28:29], v[100:101], v[28:29]
	v_pk_mul_f32 v[30:31], v[102:103], v[30:31]
	global_store_dwordx4 v[38:39], v[24:27], off nt
	global_store_dwordx4 v[38:39], v[28:31], off offset:16 nt
	s_waitcnt vmcnt(14)
	v_lshlrev_b32_e32 v144, 16, v140
	v_and_b32_e32 v145, 0xffff0000, v140
	v_lshlrev_b32_e32 v146, 16, v141
	v_and_b32_e32 v147, 0xffff0000, v141
	v_lshlrev_b32_e32 v148, 16, v142
	v_and_b32_e32 v149, 0xffff0000, v142
	v_lshlrev_b32_e32 v150, 16, v143
	v_and_b32_e32 v151, 0xffff0000, v143
	v_pk_mul_f32 v[144:145], v[0:1], v[144:145] op_sel_hi:[0,1]
	v_pk_mul_f32 v[146:147], v[0:1], v[146:147] op_sel_hi:[0,1]
	v_pk_mul_f32 v[148:149], v[0:1], v[148:149] op_sel_hi:[0,1]
	v_pk_mul_f32 v[150:151], v[0:1], v[150:151] op_sel_hi:[0,1]
	v_pk_mul_f32 v[144:145], v[104:105], v[144:145]
	v_pk_mul_f32 v[146:147], v[106:107], v[146:147]
	v_pk_mul_f32 v[148:149], v[108:109], v[148:149]
	v_pk_mul_f32 v[150:151], v[110:111], v[150:151]
	global_store_dwordx4 v[38:39], v[144:147], off offset:2048 nt
	global_store_dwordx4 v[38:39], v[148:151], off offset:2064 nt
	s_cmpk_lt_i32 s90, 0x4000
	s_cbranch_scc1 .LBB0_2434
